# EpiRes epilogue (A8,F2): XR loads batched 8-deep instead of serialized load-wait-store
# baseline (speedup 1.0000x reference)
.LBB0_1202:
	v_lshl_add_u32 v160, s24, 8, v1
	v_lshl_or_b32 v158, s25, 8, v165
	s_lshl_b64 s[20:21], s[20:21], 2
	v_ashrrev_i32_e32 v161, 31, v160
	s_add_u32 s20, s55, s20
	v_ashrrev_i32_e32 v159, 31, v158
	v_lshlrev_b64 v[162:163], 11, v[160:161]
	s_addc_u32 s21, s60, s21
	v_lshl_add_u64 v[168:169], s[10:11], 0, v[162:163]
	v_lshlrev_b64 v[162:163], 1, v[158:159]
	v_lshl_add_u64 v[68:69], v[158:159], 2, s[20:21]
	v_lshl_add_u64 v[158:159], v[168:169], 0, v[162:163]
	global_load_dwordx4 v[72:75], v[68:69], off offset:16
	global_load_dwordx4 v[80:83], v[68:69], off
	global_load_dwordx4 v[64:67], v[68:69], off offset:528
	s_nop 0
	global_load_dwordx4 v[68:71], v[68:69], off offset:512
	s_mov_b32 s15, 0x40000
	s_mov_b64 s[20:21], 0x40000
	s_mov_b64 s[24:25], -1
	s_mov_b32 s15, 0x48000
	s_mov_b32 s15, 0x50000
	s_mov_b32 s15, 0x58000
	v_mov_b32_e32 v238, 0x40000
	v_mov_b32_e32 v239, 0
	v_mov_b32_e32 v220, 0x8000
	v_mov_b32_e32 v221, 0
	v_lshl_add_u64 v[208:209], v[158:159], 0, v[220:221]
	v_lshl_add_u64 v[210:211], v[208:209], 0, v[220:221]
	v_lshl_add_u64 v[216:217], v[210:211], 0, v[220:221]
	v_lshl_add_u64 v[230:231], v[158:159], 0, v[238:239]
	v_lshl_add_u64 v[232:233], v[230:231], 0, v[220:221]
	v_lshl_add_u64 v[234:235], v[232:233], 0, v[220:221]
	v_lshl_add_u64 v[236:237], v[234:235], 0, v[220:221]
	global_load_dwordx4 v[168:171], v[158:159], off
	global_load_dwordx4 v[172:175], v[158:159], off offset:256
	global_load_dwordx4 v[176:179], v[208:209], off
	global_load_dwordx4 v[180:183], v[208:209], off offset:256
	global_load_dwordx4 v[184:187], v[210:211], off
	global_load_dwordx4 v[188:191], v[210:211], off offset:256
	global_load_dwordx4 v[192:195], v[216:217], off
	global_load_dwordx4 v[196:199], v[216:217], off offset:256
	s_waitcnt vmcnt(7)
	v_lshlrev_b32_e32 v222, 16, v168
	v_and_b32_e32 v223, 0xffff0000, v168
	v_lshlrev_b32_e32 v218, 16, v169
	v_and_b32_e32 v219, 0xffff0000, v169
	v_pk_fma_f32 v[144:145], v[144:145], v[80:81], v[222:223]
	v_pk_fma_f32 v[146:147], v[146:147], v[82:83], v[218:219]
	v_lshlrev_b32_e32 v222, 16, v170
	v_and_b32_e32 v223, 0xffff0000, v170
	v_lshlrev_b32_e32 v218, 16, v171
	v_and_b32_e32 v219, 0xffff0000, v171
	v_pk_fma_f32 v[140:141], v[140:141], v[72:73], v[222:223]
	v_pk_fma_f32 v[142:143], v[142:143], v[74:75], v[218:219]
	v_cvt_pk_bf16_f32 v168, v144, v145
	v_cvt_pk_bf16_f32 v169, v146, v147
	v_cvt_pk_bf16_f32 v170, v140, v141
	v_cvt_pk_bf16_f32 v171, v142, v143
	global_store_dwordx4 v[158:159], v[168:171], off
	s_nop 1
	global_load_dwordx4 v[168:171], v[230:231], off
	s_waitcnt vmcnt(8)
	v_lshlrev_b32_e32 v222, 16, v172
	v_and_b32_e32 v223, 0xffff0000, v172
	v_lshlrev_b32_e32 v218, 16, v173
	v_and_b32_e32 v219, 0xffff0000, v173
	v_pk_fma_f32 v[136:137], v[136:137], v[68:69], v[222:223]
	v_pk_fma_f32 v[138:139], v[138:139], v[70:71], v[218:219]
	v_lshlrev_b32_e32 v222, 16, v174
	v_and_b32_e32 v223, 0xffff0000, v174
	v_lshlrev_b32_e32 v218, 16, v175
	v_and_b32_e32 v219, 0xffff0000, v175
	v_pk_fma_f32 v[132:133], v[132:133], v[64:65], v[222:223]
	v_pk_fma_f32 v[134:135], v[134:135], v[66:67], v[218:219]
	v_cvt_pk_bf16_f32 v172, v136, v137
	v_cvt_pk_bf16_f32 v173, v138, v139
	v_cvt_pk_bf16_f32 v174, v132, v133
	v_cvt_pk_bf16_f32 v175, v134, v135
	global_store_dwordx4 v[158:159], v[172:175], off offset:256
	s_nop 1
	global_load_dwordx4 v[172:175], v[230:231], off offset:256
	s_waitcnt vmcnt(9)
	v_lshlrev_b32_e32 v222, 16, v176
	v_and_b32_e32 v223, 0xffff0000, v176
	v_lshlrev_b32_e32 v218, 16, v177
	v_and_b32_e32 v219, 0xffff0000, v177
	v_pk_fma_f32 v[128:129], v[128:129], v[80:81], v[222:223]
	v_pk_fma_f32 v[130:131], v[130:131], v[82:83], v[218:219]
	v_lshlrev_b32_e32 v222, 16, v178
	v_and_b32_e32 v223, 0xffff0000, v178
	v_lshlrev_b32_e32 v218, 16, v179
	v_and_b32_e32 v219, 0xffff0000, v179
	v_pk_fma_f32 v[124:125], v[124:125], v[72:73], v[222:223]
	v_pk_fma_f32 v[126:127], v[126:127], v[74:75], v[218:219]
	v_cvt_pk_bf16_f32 v176, v128, v129
	v_cvt_pk_bf16_f32 v177, v130, v131
	v_cvt_pk_bf16_f32 v178, v124, v125
	v_cvt_pk_bf16_f32 v179, v126, v127
	global_store_dwordx4 v[208:209], v[176:179], off
	s_nop 1
	global_load_dwordx4 v[176:179], v[232:233], off
	s_waitcnt vmcnt(10)
	v_lshlrev_b32_e32 v222, 16, v180
	v_and_b32_e32 v223, 0xffff0000, v180
	v_lshlrev_b32_e32 v218, 16, v181
	v_and_b32_e32 v219, 0xffff0000, v181
	v_pk_fma_f32 v[120:121], v[120:121], v[68:69], v[222:223]
	v_pk_fma_f32 v[122:123], v[122:123], v[70:71], v[218:219]
	v_lshlrev_b32_e32 v222, 16, v182
	v_and_b32_e32 v223, 0xffff0000, v182
	v_lshlrev_b32_e32 v218, 16, v183
	v_and_b32_e32 v219, 0xffff0000, v183
	v_pk_fma_f32 v[116:117], v[116:117], v[64:65], v[222:223]
	v_pk_fma_f32 v[118:119], v[118:119], v[66:67], v[218:219]
	v_cvt_pk_bf16_f32 v180, v120, v121
	v_cvt_pk_bf16_f32 v181, v122, v123
	v_cvt_pk_bf16_f32 v182, v116, v117
	v_cvt_pk_bf16_f32 v183, v118, v119
	global_store_dwordx4 v[208:209], v[180:183], off offset:256
	s_nop 1
	global_load_dwordx4 v[180:183], v[232:233], off offset:256
	s_waitcnt vmcnt(11)
	v_lshlrev_b32_e32 v222, 16, v184
	v_and_b32_e32 v223, 0xffff0000, v184
	v_lshlrev_b32_e32 v218, 16, v185
	v_and_b32_e32 v219, 0xffff0000, v185
	v_pk_fma_f32 v[112:113], v[112:113], v[80:81], v[222:223]
	v_pk_fma_f32 v[114:115], v[114:115], v[82:83], v[218:219]
	v_lshlrev_b32_e32 v222, 16, v186
	v_and_b32_e32 v223, 0xffff0000, v186
	v_lshlrev_b32_e32 v218, 16, v187
	v_and_b32_e32 v219, 0xffff0000, v187
	v_pk_fma_f32 v[108:109], v[108:109], v[72:73], v[222:223]
	v_pk_fma_f32 v[110:111], v[110:111], v[74:75], v[218:219]
	v_cvt_pk_bf16_f32 v184, v112, v113
	v_cvt_pk_bf16_f32 v185, v114, v115
	v_cvt_pk_bf16_f32 v186, v108, v109
	v_cvt_pk_bf16_f32 v187, v110, v111
	global_store_dwordx4 v[210:211], v[184:187], off
	s_nop 1
	global_load_dwordx4 v[184:187], v[234:235], off
	s_waitcnt vmcnt(12)
	v_lshlrev_b32_e32 v222, 16, v188
	v_and_b32_e32 v223, 0xffff0000, v188
	v_lshlrev_b32_e32 v218, 16, v189
	v_and_b32_e32 v219, 0xffff0000, v189
	v_pk_fma_f32 v[104:105], v[104:105], v[68:69], v[222:223]
	v_pk_fma_f32 v[106:107], v[106:107], v[70:71], v[218:219]
	v_lshlrev_b32_e32 v222, 16, v190
	v_and_b32_e32 v223, 0xffff0000, v190
	v_lshlrev_b32_e32 v218, 16, v191
	v_and_b32_e32 v219, 0xffff0000, v191
	v_pk_fma_f32 v[100:101], v[100:101], v[64:65], v[222:223]
	v_pk_fma_f32 v[102:103], v[102:103], v[66:67], v[218:219]
	v_cvt_pk_bf16_f32 v188, v104, v105
	v_cvt_pk_bf16_f32 v189, v106, v107
	v_cvt_pk_bf16_f32 v190, v100, v101
	v_cvt_pk_bf16_f32 v191, v102, v103
	global_store_dwordx4 v[210:211], v[188:191], off offset:256
	s_nop 1
	global_load_dwordx4 v[188:191], v[234:235], off offset:256
	s_waitcnt vmcnt(13)
	v_lshlrev_b32_e32 v222, 16, v192
	v_and_b32_e32 v223, 0xffff0000, v192
	v_lshlrev_b32_e32 v218, 16, v193
	v_and_b32_e32 v219, 0xffff0000, v193
	v_pk_fma_f32 v[96:97], v[96:97], v[80:81], v[222:223]
	v_pk_fma_f32 v[98:99], v[98:99], v[82:83], v[218:219]
	v_lshlrev_b32_e32 v222, 16, v194
	v_and_b32_e32 v223, 0xffff0000, v194
	v_lshlrev_b32_e32 v218, 16, v195
	v_and_b32_e32 v219, 0xffff0000, v195
	v_pk_fma_f32 v[92:93], v[92:93], v[72:73], v[222:223]
	v_pk_fma_f32 v[94:95], v[94:95], v[74:75], v[218:219]
	v_cvt_pk_bf16_f32 v192, v96, v97
	v_cvt_pk_bf16_f32 v193, v98, v99
	v_cvt_pk_bf16_f32 v194, v92, v93
	v_cvt_pk_bf16_f32 v195, v94, v95
	global_store_dwordx4 v[216:217], v[192:195], off
	s_nop 1
	global_load_dwordx4 v[192:195], v[236:237], off
	s_waitcnt vmcnt(14)
	v_lshlrev_b32_e32 v222, 16, v196
	v_and_b32_e32 v223, 0xffff0000, v196
	v_lshlrev_b32_e32 v218, 16, v197
	v_and_b32_e32 v219, 0xffff0000, v197
	v_pk_fma_f32 v[88:89], v[88:89], v[68:69], v[222:223]
	v_pk_fma_f32 v[90:91], v[90:91], v[70:71], v[218:219]
	v_lshlrev_b32_e32 v222, 16, v198
	v_and_b32_e32 v223, 0xffff0000, v198
	v_lshlrev_b32_e32 v218, 16, v199
	v_and_b32_e32 v219, 0xffff0000, v199
	v_pk_fma_f32 v[84:85], v[84:85], v[64:65], v[222:223]
	v_pk_fma_f32 v[86:87], v[86:87], v[66:67], v[218:219]
	v_cvt_pk_bf16_f32 v196, v88, v89
	v_cvt_pk_bf16_f32 v197, v90, v91
	v_cvt_pk_bf16_f32 v198, v84, v85
	v_cvt_pk_bf16_f32 v199, v86, v87
	global_store_dwordx4 v[216:217], v[196:199], off offset:256
	s_nop 1
	global_load_dwordx4 v[196:199], v[236:237], off offset:256
	s_waitcnt vmcnt(14)
	v_lshlrev_b32_e32 v222, 16, v168
	v_and_b32_e32 v223, 0xffff0000, v168
	v_lshlrev_b32_e32 v218, 16, v169
	v_and_b32_e32 v219, 0xffff0000, v169
	v_pk_fma_f32 v[76:77], v[76:77], v[80:81], v[222:223]
	v_pk_fma_f32 v[78:79], v[78:79], v[82:83], v[218:219]
	v_lshlrev_b32_e32 v222, 16, v170
	v_and_b32_e32 v223, 0xffff0000, v170
	v_lshlrev_b32_e32 v218, 16, v171
	v_and_b32_e32 v219, 0xffff0000, v171
	v_pk_fma_f32 v[60:61], v[60:61], v[72:73], v[222:223]
	v_pk_fma_f32 v[62:63], v[62:63], v[74:75], v[218:219]
	v_cvt_pk_bf16_f32 v168, v76, v77
	v_cvt_pk_bf16_f32 v169, v78, v79
	v_cvt_pk_bf16_f32 v170, v60, v61
	v_cvt_pk_bf16_f32 v171, v62, v63
	global_store_dwordx4 v[230:231], v[168:171], off
	s_waitcnt vmcnt(13)
	v_lshlrev_b32_e32 v222, 16, v172
	v_and_b32_e32 v223, 0xffff0000, v172
	v_lshlrev_b32_e32 v218, 16, v173
	v_and_b32_e32 v219, 0xffff0000, v173
	v_pk_fma_f32 v[56:57], v[56:57], v[68:69], v[222:223]
	v_pk_fma_f32 v[58:59], v[58:59], v[70:71], v[218:219]
	v_lshlrev_b32_e32 v222, 16, v174
	v_and_b32_e32 v223, 0xffff0000, v174
	v_lshlrev_b32_e32 v218, 16, v175
	v_and_b32_e32 v219, 0xffff0000, v175
	v_pk_fma_f32 v[52:53], v[52:53], v[64:65], v[222:223]
	v_pk_fma_f32 v[54:55], v[54:55], v[66:67], v[218:219]
	v_cvt_pk_bf16_f32 v172, v56, v57
	v_cvt_pk_bf16_f32 v173, v58, v59
	v_cvt_pk_bf16_f32 v174, v52, v53
	v_cvt_pk_bf16_f32 v175, v54, v55
	global_store_dwordx4 v[230:231], v[172:175], off offset:256
	s_waitcnt vmcnt(12)
	v_lshlrev_b32_e32 v222, 16, v176
	v_and_b32_e32 v223, 0xffff0000, v176
	v_lshlrev_b32_e32 v218, 16, v177
	v_and_b32_e32 v219, 0xffff0000, v177
	v_pk_fma_f32 v[48:49], v[48:49], v[80:81], v[222:223]
	v_pk_fma_f32 v[50:51], v[50:51], v[82:83], v[218:219]
	v_lshlrev_b32_e32 v222, 16, v178
	v_and_b32_e32 v223, 0xffff0000, v178
	v_lshlrev_b32_e32 v218, 16, v179
	v_and_b32_e32 v219, 0xffff0000, v179
	v_pk_fma_f32 v[44:45], v[44:45], v[72:73], v[222:223]
	v_pk_fma_f32 v[46:47], v[46:47], v[74:75], v[218:219]
	v_cvt_pk_bf16_f32 v176, v48, v49
	v_cvt_pk_bf16_f32 v177, v50, v51
	v_cvt_pk_bf16_f32 v178, v44, v45
	v_cvt_pk_bf16_f32 v179, v46, v47
	global_store_dwordx4 v[232:233], v[176:179], off
	s_waitcnt vmcnt(11)
	v_lshlrev_b32_e32 v222, 16, v180
	v_and_b32_e32 v223, 0xffff0000, v180
	v_lshlrev_b32_e32 v218, 16, v181
	v_and_b32_e32 v219, 0xffff0000, v181
	v_pk_fma_f32 v[40:41], v[40:41], v[68:69], v[222:223]
	v_pk_fma_f32 v[42:43], v[42:43], v[70:71], v[218:219]
	v_lshlrev_b32_e32 v222, 16, v182
	v_and_b32_e32 v223, 0xffff0000, v182
	v_lshlrev_b32_e32 v218, 16, v183
	v_and_b32_e32 v219, 0xffff0000, v183
	v_pk_fma_f32 v[36:37], v[36:37], v[64:65], v[222:223]
	v_pk_fma_f32 v[38:39], v[38:39], v[66:67], v[218:219]
	v_cvt_pk_bf16_f32 v180, v40, v41
	v_cvt_pk_bf16_f32 v181, v42, v43
	v_cvt_pk_bf16_f32 v182, v36, v37
	v_cvt_pk_bf16_f32 v183, v38, v39
	global_store_dwordx4 v[232:233], v[180:183], off offset:256
	s_waitcnt vmcnt(10)
	v_lshlrev_b32_e32 v222, 16, v184
	v_and_b32_e32 v223, 0xffff0000, v184
	v_lshlrev_b32_e32 v218, 16, v185
	v_and_b32_e32 v219, 0xffff0000, v185
	v_pk_fma_f32 v[32:33], v[32:33], v[80:81], v[222:223]
	v_pk_fma_f32 v[34:35], v[34:35], v[82:83], v[218:219]
	v_lshlrev_b32_e32 v222, 16, v186
	v_and_b32_e32 v223, 0xffff0000, v186
	v_lshlrev_b32_e32 v218, 16, v187
	v_and_b32_e32 v219, 0xffff0000, v187
	v_pk_fma_f32 v[28:29], v[28:29], v[72:73], v[222:223]
	v_pk_fma_f32 v[30:31], v[30:31], v[74:75], v[218:219]
	v_cvt_pk_bf16_f32 v184, v32, v33
	v_cvt_pk_bf16_f32 v185, v34, v35
	v_cvt_pk_bf16_f32 v186, v28, v29
	v_cvt_pk_bf16_f32 v187, v30, v31
	global_store_dwordx4 v[234:235], v[184:187], off
	s_waitcnt vmcnt(9)
	v_lshlrev_b32_e32 v222, 16, v188
	v_and_b32_e32 v223, 0xffff0000, v188
	v_lshlrev_b32_e32 v218, 16, v189
	v_and_b32_e32 v219, 0xffff0000, v189
	v_pk_fma_f32 v[24:25], v[24:25], v[68:69], v[222:223]
	v_pk_fma_f32 v[26:27], v[26:27], v[70:71], v[218:219]
	v_lshlrev_b32_e32 v222, 16, v190
	v_and_b32_e32 v223, 0xffff0000, v190
	v_lshlrev_b32_e32 v218, 16, v191
	v_and_b32_e32 v219, 0xffff0000, v191
	v_pk_fma_f32 v[20:21], v[20:21], v[64:65], v[222:223]
	v_pk_fma_f32 v[22:23], v[22:23], v[66:67], v[218:219]
	v_cvt_pk_bf16_f32 v188, v24, v25
	v_cvt_pk_bf16_f32 v189, v26, v27
	v_cvt_pk_bf16_f32 v190, v20, v21
	v_cvt_pk_bf16_f32 v191, v22, v23
	global_store_dwordx4 v[234:235], v[188:191], off offset:256
	s_waitcnt vmcnt(8)
	v_lshlrev_b32_e32 v222, 16, v192
	v_and_b32_e32 v223, 0xffff0000, v192
	v_lshlrev_b32_e32 v218, 16, v193
	v_and_b32_e32 v219, 0xffff0000, v193
	v_pk_fma_f32 v[16:17], v[16:17], v[80:81], v[222:223]
	v_pk_fma_f32 v[18:19], v[18:19], v[82:83], v[218:219]
	v_lshlrev_b32_e32 v222, 16, v194
	v_and_b32_e32 v223, 0xffff0000, v194
	v_lshlrev_b32_e32 v218, 16, v195
	v_and_b32_e32 v219, 0xffff0000, v195
	v_pk_fma_f32 v[12:13], v[12:13], v[72:73], v[222:223]
	v_pk_fma_f32 v[14:15], v[14:15], v[74:75], v[218:219]
	v_cvt_pk_bf16_f32 v192, v16, v17
	v_cvt_pk_bf16_f32 v193, v18, v19
	v_cvt_pk_bf16_f32 v194, v12, v13
	v_cvt_pk_bf16_f32 v195, v14, v15
	global_store_dwordx4 v[236:237], v[192:195], off
	s_waitcnt vmcnt(7)
	v_lshlrev_b32_e32 v222, 16, v196
	v_and_b32_e32 v223, 0xffff0000, v196
	v_lshlrev_b32_e32 v218, 16, v197
	v_and_b32_e32 v219, 0xffff0000, v197
	v_pk_fma_f32 v[8:9], v[8:9], v[68:69], v[222:223]
	v_pk_fma_f32 v[10:11], v[10:11], v[70:71], v[218:219]
	v_lshlrev_b32_e32 v222, 16, v198
	v_and_b32_e32 v223, 0xffff0000, v198
	v_lshlrev_b32_e32 v218, 16, v199
	v_and_b32_e32 v219, 0xffff0000, v199
	v_pk_fma_f32 v[4:5], v[4:5], v[64:65], v[222:223]
	v_pk_fma_f32 v[6:7], v[6:7], v[66:67], v[218:219]
	v_cvt_pk_bf16_f32 v196, v8, v9
	v_cvt_pk_bf16_f32 v197, v10, v11
	v_cvt_pk_bf16_f32 v198, v4, v5
	v_cvt_pk_bf16_f32 v199, v6, v7
	global_store_dwordx4 v[236:237], v[196:199], off offset:256
	s_andn2_b64 vcc, exec, s[4:5]
	s_cbranch_vccnz .LBB0_1192
	s_andn2_b64 vcc, exec, s[8:9]
	s_cbranch_vccnz .LBB0_1191
	s_barrier
	s_branch .LBB0_1191

.LBB0_1778:
	v_lshl_add_u32 v160, s53, 8, v1
	v_lshl_or_b32 v158, s54, 8, v165
	s_lshl_b64 s[18:19], s[18:19], 2
	v_ashrrev_i32_e32 v161, 31, v160
	s_add_u32 s18, s36, s18
	v_ashrrev_i32_e32 v159, 31, v158
	v_lshlrev_b64 v[162:163], 11, v[160:161]
	s_addc_u32 s19, s46, s19
	v_lshl_add_u64 v[168:169], s[12:13], 0, v[162:163]
	v_lshlrev_b64 v[162:163], 1, v[158:159]
	v_lshl_add_u64 v[68:69], v[158:159], 2, s[18:19]
	v_lshl_add_u64 v[158:159], v[168:169], 0, v[162:163]
	global_load_dwordx4 v[72:75], v[68:69], off offset:16
	global_load_dwordx4 v[80:83], v[68:69], off
	global_load_dwordx4 v[64:67], v[68:69], off offset:528
	s_nop 0
	global_load_dwordx4 v[68:71], v[68:69], off offset:512
	s_mov_b64 s[18:19], 0x40000
	s_mov_b32 s18, 0x40000
	s_mov_b32 s18, 0x48000
	s_mov_b32 s18, 0x50000
	s_mov_b32 s18, 0x58000
	s_mov_b64 s[18:19], -1
	v_mov_b32_e32 v238, 0x40000
	v_mov_b32_e32 v239, 0
	v_mov_b32_e32 v220, 0x8000
	v_mov_b32_e32 v221, 0
	v_lshl_add_u64 v[208:209], v[158:159], 0, v[220:221]
	v_lshl_add_u64 v[210:211], v[208:209], 0, v[220:221]
	v_lshl_add_u64 v[216:217], v[210:211], 0, v[220:221]
	v_lshl_add_u64 v[230:231], v[158:159], 0, v[238:239]
	v_lshl_add_u64 v[232:233], v[230:231], 0, v[220:221]
	v_lshl_add_u64 v[234:235], v[232:233], 0, v[220:221]
	v_lshl_add_u64 v[236:237], v[234:235], 0, v[220:221]
	global_load_dwordx4 v[168:171], v[158:159], off
	global_load_dwordx4 v[172:175], v[158:159], off offset:256
	global_load_dwordx4 v[176:179], v[208:209], off
	global_load_dwordx4 v[180:183], v[208:209], off offset:256
	global_load_dwordx4 v[184:187], v[210:211], off
	global_load_dwordx4 v[188:191], v[210:211], off offset:256
	global_load_dwordx4 v[192:195], v[216:217], off
	global_load_dwordx4 v[196:199], v[216:217], off offset:256
	s_waitcnt vmcnt(7)
	v_lshlrev_b32_e32 v222, 16, v168
	v_and_b32_e32 v223, 0xffff0000, v168
	v_lshlrev_b32_e32 v218, 16, v169
	v_and_b32_e32 v219, 0xffff0000, v169
	v_pk_fma_f32 v[144:145], v[144:145], v[80:81], v[222:223]
	v_pk_fma_f32 v[146:147], v[146:147], v[82:83], v[218:219]
	v_lshlrev_b32_e32 v222, 16, v170
	v_and_b32_e32 v223, 0xffff0000, v170
	v_lshlrev_b32_e32 v218, 16, v171
	v_and_b32_e32 v219, 0xffff0000, v171
	v_pk_fma_f32 v[140:141], v[140:141], v[72:73], v[222:223]
	v_pk_fma_f32 v[142:143], v[142:143], v[74:75], v[218:219]
	v_cvt_pk_bf16_f32 v168, v144, v145
	v_cvt_pk_bf16_f32 v169, v146, v147
	v_cvt_pk_bf16_f32 v170, v140, v141
	v_cvt_pk_bf16_f32 v171, v142, v143
	global_store_dwordx4 v[158:159], v[168:171], off
	s_nop 1
	global_load_dwordx4 v[168:171], v[230:231], off
	s_waitcnt vmcnt(8)
	v_lshlrev_b32_e32 v222, 16, v172
	v_and_b32_e32 v223, 0xffff0000, v172
	v_lshlrev_b32_e32 v218, 16, v173
	v_and_b32_e32 v219, 0xffff0000, v173
	v_pk_fma_f32 v[136:137], v[136:137], v[68:69], v[222:223]
	v_pk_fma_f32 v[138:139], v[138:139], v[70:71], v[218:219]
	v_lshlrev_b32_e32 v222, 16, v174
	v_and_b32_e32 v223, 0xffff0000, v174
	v_lshlrev_b32_e32 v218, 16, v175
	v_and_b32_e32 v219, 0xffff0000, v175
	v_pk_fma_f32 v[132:133], v[132:133], v[64:65], v[222:223]
	v_pk_fma_f32 v[134:135], v[134:135], v[66:67], v[218:219]
	v_cvt_pk_bf16_f32 v172, v136, v137
	v_cvt_pk_bf16_f32 v173, v138, v139
	v_cvt_pk_bf16_f32 v174, v132, v133
	v_cvt_pk_bf16_f32 v175, v134, v135
	global_store_dwordx4 v[158:159], v[172:175], off offset:256
	s_nop 1
	global_load_dwordx4 v[172:175], v[230:231], off offset:256
	s_waitcnt vmcnt(9)
	v_lshlrev_b32_e32 v222, 16, v176
	v_and_b32_e32 v223, 0xffff0000, v176
	v_lshlrev_b32_e32 v218, 16, v177
	v_and_b32_e32 v219, 0xffff0000, v177
	v_pk_fma_f32 v[128:129], v[128:129], v[80:81], v[222:223]
	v_pk_fma_f32 v[130:131], v[130:131], v[82:83], v[218:219]
	v_lshlrev_b32_e32 v222, 16, v178
	v_and_b32_e32 v223, 0xffff0000, v178
	v_lshlrev_b32_e32 v218, 16, v179
	v_and_b32_e32 v219, 0xffff0000, v179
	v_pk_fma_f32 v[124:125], v[124:125], v[72:73], v[222:223]
	v_pk_fma_f32 v[126:127], v[126:127], v[74:75], v[218:219]
	v_cvt_pk_bf16_f32 v176, v128, v129
	v_cvt_pk_bf16_f32 v177, v130, v131
	v_cvt_pk_bf16_f32 v178, v124, v125
	v_cvt_pk_bf16_f32 v179, v126, v127
	global_store_dwordx4 v[208:209], v[176:179], off
	s_nop 1
	global_load_dwordx4 v[176:179], v[232:233], off
	s_waitcnt vmcnt(10)
	v_lshlrev_b32_e32 v222, 16, v180
	v_and_b32_e32 v223, 0xffff0000, v180
	v_lshlrev_b32_e32 v218, 16, v181
	v_and_b32_e32 v219, 0xffff0000, v181
	v_pk_fma_f32 v[120:121], v[120:121], v[68:69], v[222:223]
	v_pk_fma_f32 v[122:123], v[122:123], v[70:71], v[218:219]
	v_lshlrev_b32_e32 v222, 16, v182
	v_and_b32_e32 v223, 0xffff0000, v182
	v_lshlrev_b32_e32 v218, 16, v183
	v_and_b32_e32 v219, 0xffff0000, v183
	v_pk_fma_f32 v[116:117], v[116:117], v[64:65], v[222:223]
	v_pk_fma_f32 v[118:119], v[118:119], v[66:67], v[218:219]
	v_cvt_pk_bf16_f32 v180, v120, v121
	v_cvt_pk_bf16_f32 v181, v122, v123
	v_cvt_pk_bf16_f32 v182, v116, v117
	v_cvt_pk_bf16_f32 v183, v118, v119
	global_store_dwordx4 v[208:209], v[180:183], off offset:256
	s_nop 1
	global_load_dwordx4 v[180:183], v[232:233], off offset:256
	s_waitcnt vmcnt(11)
	v_lshlrev_b32_e32 v222, 16, v184
	v_and_b32_e32 v223, 0xffff0000, v184
	v_lshlrev_b32_e32 v218, 16, v185
	v_and_b32_e32 v219, 0xffff0000, v185
	v_pk_fma_f32 v[112:113], v[112:113], v[80:81], v[222:223]
	v_pk_fma_f32 v[114:115], v[114:115], v[82:83], v[218:219]
	v_lshlrev_b32_e32 v222, 16, v186
	v_and_b32_e32 v223, 0xffff0000, v186
	v_lshlrev_b32_e32 v218, 16, v187
	v_and_b32_e32 v219, 0xffff0000, v187
	v_pk_fma_f32 v[108:109], v[108:109], v[72:73], v[222:223]
	v_pk_fma_f32 v[110:111], v[110:111], v[74:75], v[218:219]
	v_cvt_pk_bf16_f32 v184, v112, v113
	v_cvt_pk_bf16_f32 v185, v114, v115
	v_cvt_pk_bf16_f32 v186, v108, v109
	v_cvt_pk_bf16_f32 v187, v110, v111
	global_store_dwordx4 v[210:211], v[184:187], off
	s_nop 1
	global_load_dwordx4 v[184:187], v[234:235], off
	s_waitcnt vmcnt(12)
	v_lshlrev_b32_e32 v222, 16, v188
	v_and_b32_e32 v223, 0xffff0000, v188
	v_lshlrev_b32_e32 v218, 16, v189
	v_and_b32_e32 v219, 0xffff0000, v189
	v_pk_fma_f32 v[104:105], v[104:105], v[68:69], v[222:223]
	v_pk_fma_f32 v[106:107], v[106:107], v[70:71], v[218:219]
	v_lshlrev_b32_e32 v222, 16, v190
	v_and_b32_e32 v223, 0xffff0000, v190
	v_lshlrev_b32_e32 v218, 16, v191
	v_and_b32_e32 v219, 0xffff0000, v191
	v_pk_fma_f32 v[100:101], v[100:101], v[64:65], v[222:223]
	v_pk_fma_f32 v[102:103], v[102:103], v[66:67], v[218:219]
	v_cvt_pk_bf16_f32 v188, v104, v105
	v_cvt_pk_bf16_f32 v189, v106, v107
	v_cvt_pk_bf16_f32 v190, v100, v101
	v_cvt_pk_bf16_f32 v191, v102, v103
	global_store_dwordx4 v[210:211], v[188:191], off offset:256
	s_nop 1
	global_load_dwordx4 v[188:191], v[234:235], off offset:256
	s_waitcnt vmcnt(13)
	v_lshlrev_b32_e32 v222, 16, v192
	v_and_b32_e32 v223, 0xffff0000, v192
	v_lshlrev_b32_e32 v218, 16, v193
	v_and_b32_e32 v219, 0xffff0000, v193
	v_pk_fma_f32 v[96:97], v[96:97], v[80:81], v[222:223]
	v_pk_fma_f32 v[98:99], v[98:99], v[82:83], v[218:219]
	v_lshlrev_b32_e32 v222, 16, v194
	v_and_b32_e32 v223, 0xffff0000, v194
	v_lshlrev_b32_e32 v218, 16, v195
	v_and_b32_e32 v219, 0xffff0000, v195
	v_pk_fma_f32 v[92:93], v[92:93], v[72:73], v[222:223]
	v_pk_fma_f32 v[94:95], v[94:95], v[74:75], v[218:219]
	v_cvt_pk_bf16_f32 v192, v96, v97
	v_cvt_pk_bf16_f32 v193, v98, v99
	v_cvt_pk_bf16_f32 v194, v92, v93
	v_cvt_pk_bf16_f32 v195, v94, v95
	global_store_dwordx4 v[216:217], v[192:195], off
	s_nop 1
	global_load_dwordx4 v[192:195], v[236:237], off
	s_waitcnt vmcnt(14)
	v_lshlrev_b32_e32 v222, 16, v196
	v_and_b32_e32 v223, 0xffff0000, v196
	v_lshlrev_b32_e32 v218, 16, v197
	v_and_b32_e32 v219, 0xffff0000, v197
	v_pk_fma_f32 v[88:89], v[88:89], v[68:69], v[222:223]
	v_pk_fma_f32 v[90:91], v[90:91], v[70:71], v[218:219]
	v_lshlrev_b32_e32 v222, 16, v198
	v_and_b32_e32 v223, 0xffff0000, v198
	v_lshlrev_b32_e32 v218, 16, v199
	v_and_b32_e32 v219, 0xffff0000, v199
	v_pk_fma_f32 v[84:85], v[84:85], v[64:65], v[222:223]
	v_pk_fma_f32 v[86:87], v[86:87], v[66:67], v[218:219]
	v_cvt_pk_bf16_f32 v196, v88, v89
	v_cvt_pk_bf16_f32 v197, v90, v91
	v_cvt_pk_bf16_f32 v198, v84, v85
	v_cvt_pk_bf16_f32 v199, v86, v87
	global_store_dwordx4 v[216:217], v[196:199], off offset:256
	s_nop 1
	global_load_dwordx4 v[196:199], v[236:237], off offset:256
	s_waitcnt vmcnt(14)
	v_lshlrev_b32_e32 v222, 16, v168
	v_and_b32_e32 v223, 0xffff0000, v168
	v_lshlrev_b32_e32 v218, 16, v169
	v_and_b32_e32 v219, 0xffff0000, v169
	v_pk_fma_f32 v[76:77], v[76:77], v[80:81], v[222:223]
	v_pk_fma_f32 v[78:79], v[78:79], v[82:83], v[218:219]
	v_lshlrev_b32_e32 v222, 16, v170
	v_and_b32_e32 v223, 0xffff0000, v170
	v_lshlrev_b32_e32 v218, 16, v171
	v_and_b32_e32 v219, 0xffff0000, v171
	v_pk_fma_f32 v[60:61], v[60:61], v[72:73], v[222:223]
	v_pk_fma_f32 v[62:63], v[62:63], v[74:75], v[218:219]
	v_cvt_pk_bf16_f32 v168, v76, v77
	v_cvt_pk_bf16_f32 v169, v78, v79
	v_cvt_pk_bf16_f32 v170, v60, v61
	v_cvt_pk_bf16_f32 v171, v62, v63
	global_store_dwordx4 v[230:231], v[168:171], off
	s_waitcnt vmcnt(13)
	v_lshlrev_b32_e32 v222, 16, v172
	v_and_b32_e32 v223, 0xffff0000, v172
	v_lshlrev_b32_e32 v218, 16, v173
	v_and_b32_e32 v219, 0xffff0000, v173
	v_pk_fma_f32 v[56:57], v[56:57], v[68:69], v[222:223]
	v_pk_fma_f32 v[58:59], v[58:59], v[70:71], v[218:219]
	v_lshlrev_b32_e32 v222, 16, v174
	v_and_b32_e32 v223, 0xffff0000, v174
	v_lshlrev_b32_e32 v218, 16, v175
	v_and_b32_e32 v219, 0xffff0000, v175
	v_pk_fma_f32 v[52:53], v[52:53], v[64:65], v[222:223]
	v_pk_fma_f32 v[54:55], v[54:55], v[66:67], v[218:219]
	v_cvt_pk_bf16_f32 v172, v56, v57
	v_cvt_pk_bf16_f32 v173, v58, v59
	v_cvt_pk_bf16_f32 v174, v52, v53
	v_cvt_pk_bf16_f32 v175, v54, v55
	global_store_dwordx4 v[230:231], v[172:175], off offset:256
	s_waitcnt vmcnt(12)
	v_lshlrev_b32_e32 v222, 16, v176
	v_and_b32_e32 v223, 0xffff0000, v176
	v_lshlrev_b32_e32 v218, 16, v177
	v_and_b32_e32 v219, 0xffff0000, v177
	v_pk_fma_f32 v[48:49], v[48:49], v[80:81], v[222:223]
	v_pk_fma_f32 v[50:51], v[50:51], v[82:83], v[218:219]
	v_lshlrev_b32_e32 v222, 16, v178
	v_and_b32_e32 v223, 0xffff0000, v178
	v_lshlrev_b32_e32 v218, 16, v179
	v_and_b32_e32 v219, 0xffff0000, v179
	v_pk_fma_f32 v[44:45], v[44:45], v[72:73], v[222:223]
	v_pk_fma_f32 v[46:47], v[46:47], v[74:75], v[218:219]
	v_cvt_pk_bf16_f32 v176, v48, v49
	v_cvt_pk_bf16_f32 v177, v50, v51
	v_cvt_pk_bf16_f32 v178, v44, v45
	v_cvt_pk_bf16_f32 v179, v46, v47
	global_store_dwordx4 v[232:233], v[176:179], off
	s_waitcnt vmcnt(11)
	v_lshlrev_b32_e32 v222, 16, v180
	v_and_b32_e32 v223, 0xffff0000, v180
	v_lshlrev_b32_e32 v218, 16, v181
	v_and_b32_e32 v219, 0xffff0000, v181
	v_pk_fma_f32 v[40:41], v[40:41], v[68:69], v[222:223]
	v_pk_fma_f32 v[42:43], v[42:43], v[70:71], v[218:219]
	v_lshlrev_b32_e32 v222, 16, v182
	v_and_b32_e32 v223, 0xffff0000, v182
	v_lshlrev_b32_e32 v218, 16, v183
	v_and_b32_e32 v219, 0xffff0000, v183
	v_pk_fma_f32 v[36:37], v[36:37], v[64:65], v[222:223]
	v_pk_fma_f32 v[38:39], v[38:39], v[66:67], v[218:219]
	v_cvt_pk_bf16_f32 v180, v40, v41
	v_cvt_pk_bf16_f32 v181, v42, v43
	v_cvt_pk_bf16_f32 v182, v36, v37
	v_cvt_pk_bf16_f32 v183, v38, v39
	global_store_dwordx4 v[232:233], v[180:183], off offset:256
	s_waitcnt vmcnt(10)
	v_lshlrev_b32_e32 v222, 16, v184
	v_and_b32_e32 v223, 0xffff0000, v184
	v_lshlrev_b32_e32 v218, 16, v185
	v_and_b32_e32 v219, 0xffff0000, v185
	v_pk_fma_f32 v[32:33], v[32:33], v[80:81], v[222:223]
	v_pk_fma_f32 v[34:35], v[34:35], v[82:83], v[218:219]
	v_lshlrev_b32_e32 v222, 16, v186
	v_and_b32_e32 v223, 0xffff0000, v186
	v_lshlrev_b32_e32 v218, 16, v187
	v_and_b32_e32 v219, 0xffff0000, v187
	v_pk_fma_f32 v[28:29], v[28:29], v[72:73], v[222:223]
	v_pk_fma_f32 v[30:31], v[30:31], v[74:75], v[218:219]
	v_cvt_pk_bf16_f32 v184, v32, v33
	v_cvt_pk_bf16_f32 v185, v34, v35
	v_cvt_pk_bf16_f32 v186, v28, v29
	v_cvt_pk_bf16_f32 v187, v30, v31
	global_store_dwordx4 v[234:235], v[184:187], off
	s_waitcnt vmcnt(9)
	v_lshlrev_b32_e32 v222, 16, v188
	v_and_b32_e32 v223, 0xffff0000, v188
	v_lshlrev_b32_e32 v218, 16, v189
	v_and_b32_e32 v219, 0xffff0000, v189
	v_pk_fma_f32 v[24:25], v[24:25], v[68:69], v[222:223]
	v_pk_fma_f32 v[26:27], v[26:27], v[70:71], v[218:219]
	v_lshlrev_b32_e32 v222, 16, v190
	v_and_b32_e32 v223, 0xffff0000, v190
	v_lshlrev_b32_e32 v218, 16, v191
	v_and_b32_e32 v219, 0xffff0000, v191
	v_pk_fma_f32 v[20:21], v[20:21], v[64:65], v[222:223]
	v_pk_fma_f32 v[22:23], v[22:23], v[66:67], v[218:219]
	v_cvt_pk_bf16_f32 v188, v24, v25
	v_cvt_pk_bf16_f32 v189, v26, v27
	v_cvt_pk_bf16_f32 v190, v20, v21
	v_cvt_pk_bf16_f32 v191, v22, v23
	global_store_dwordx4 v[234:235], v[188:191], off offset:256
	s_waitcnt vmcnt(8)
	v_lshlrev_b32_e32 v222, 16, v192
	v_and_b32_e32 v223, 0xffff0000, v192
	v_lshlrev_b32_e32 v218, 16, v193
	v_and_b32_e32 v219, 0xffff0000, v193
	v_pk_fma_f32 v[16:17], v[16:17], v[80:81], v[222:223]
	v_pk_fma_f32 v[18:19], v[18:19], v[82:83], v[218:219]
	v_lshlrev_b32_e32 v222, 16, v194
	v_and_b32_e32 v223, 0xffff0000, v194
	v_lshlrev_b32_e32 v218, 16, v195
	v_and_b32_e32 v219, 0xffff0000, v195
	v_pk_fma_f32 v[12:13], v[12:13], v[72:73], v[222:223]
	v_pk_fma_f32 v[14:15], v[14:15], v[74:75], v[218:219]
	v_cvt_pk_bf16_f32 v192, v16, v17
	v_cvt_pk_bf16_f32 v193, v18, v19
	v_cvt_pk_bf16_f32 v194, v12, v13
	v_cvt_pk_bf16_f32 v195, v14, v15
	global_store_dwordx4 v[236:237], v[192:195], off
	s_waitcnt vmcnt(7)
	v_lshlrev_b32_e32 v222, 16, v196
	v_and_b32_e32 v223, 0xffff0000, v196
	v_lshlrev_b32_e32 v218, 16, v197
	v_and_b32_e32 v219, 0xffff0000, v197
	v_pk_fma_f32 v[8:9], v[8:9], v[68:69], v[222:223]
	v_pk_fma_f32 v[10:11], v[10:11], v[70:71], v[218:219]
	v_lshlrev_b32_e32 v222, 16, v198
	v_and_b32_e32 v223, 0xffff0000, v198
	v_lshlrev_b32_e32 v218, 16, v199
	v_and_b32_e32 v219, 0xffff0000, v199
	v_pk_fma_f32 v[4:5], v[4:5], v[64:65], v[222:223]
	v_pk_fma_f32 v[6:7], v[6:7], v[66:67], v[218:219]
	v_cvt_pk_bf16_f32 v196, v8, v9
	v_cvt_pk_bf16_f32 v197, v10, v11
	v_cvt_pk_bf16_f32 v198, v4, v5
	v_cvt_pk_bf16_f32 v199, v6, v7
	global_store_dwordx4 v[236:237], v[196:199], off offset:256
	s_and_b64 vcc, exec, s[4:5]
	s_cbranch_vccnz .LBB0_1764
	s_andn2_b64 vcc, exec, s[10:11]
	s_cbranch_vccnz .LBB0_1763
	s_barrier
	s_branch .LBB0_1763
